# MLA steady-state loops: single loop-limit compare per iteration, dead s_nop dropped
# baseline (speedup 1.0000x reference)
; #define ISSUE_K(t, sl) do { glds16(Kg + (long)(t) * (KSLOT / 2), (unsigned)__builtin_amdgcn_readfirstlane(kdst + (sl) * KSLOT)); \
;         if (k2) glds16(Kg + (long)(t) * (KSLOT / 2) + 4096, (unsigned)__builtin_amdgcn_readfirstlane(kdst + (sl) * KSLOT + 8192)); } while (0)
; #define ISSUE_V(t, sl) glds16(Vg + (long)(t) * 4096, (unsigned)__builtin_amdgcn_readfirstlane(vdst + (sl) * VSLOT))
; #define SFENCE() __builtin_amdgcn_sched_barrier(0)
; template <bool FOX>
; __device__ __forceinline__ void attn_unit(const Args& A, int b, int h, int qb, LAS char* shm, LAS float* dg) {
;     ...
;     const int t_end = (tw_last - t0 + 2 < nti) ? tw_last - t0 + 2 : nti;
; #pragma unroll 1
;     for (int t = 1; t < t_end; ++t) {
;         if (t == 1 && 4 < nti) ISSUE_K(t0 + 4, 0);
;         if (t + 4 < nti) ISSUE_K(t0 + t + 4, t % NS);
;         if (t + 2 < nti) ISSUE_V(t0 + t + 2, (t + 2) % NS);
;         SFENCE();
.LBB0_825:
	s_add_i32 s27, s26, 3
	s_cmp_lt_u32 s27, s94
	s_cbranch_scc0 .LBB0_828
	s_cmp_lg_u32 s98, 0
	s_cbranch_scc0 .Lmla_ss_no
	s_cmp_lg_u32 s26, s59
	s_cbranch_scc0 .Lmla_ss_no
	s_add_i32 s47, s94, -3
	s_min_u32 s47, s47, s96
	s_cmp_lt_i32 s89, 4
	s_cbranch_scc1 .Lmla_ss1_top
	s_branch .Lmla_ss2_top

; template <bool FOX>
; __device__ __forceinline__ void attn_unit(const Args& A, int b, int h, int qb, LAS char* shm, LAS float* dg) {
;     ...
;     for (int t = 1; t < t_end; ++t) {
;         if (t == 1 && 4 < nti) ISSUE_K(t0 + 4, 0);
;         if (t + 4 < nti) ISSUE_K(t0 + t + 4, t % NS);
;         if (t + 2 < nti) ISSUE_V(t0 + t + 2, (t + 2) % NS);
;         SFENCE();
;         { if constexpr (!FOX) { if (t0 + t == tw_last + 1) {
; #pragma unroll
;                   for (int r = 0; r < 16; ++r) negm[r] = -INFINITY;
;                   asm volatile("" : "+v"(negm)); } }
;           const lds_cptr vp = vp0 + ((t - 1) % NS) * VSLOT; float sa = 0.f, sb = 0.f;
; #pragma unroll
;           for (int g = 0; g < 2 * NQ; ++g) {
;               if (!FOX && g == 0) c0 = __builtin_amdgcn_mfma_f32_32x32x16_bf16(kf[0], qr[0], negm, 0, 0, 0);
;               else if (!FOX && g == 1) c1 = __builtin_amdgcn_mfma_f32_32x32x16_bf16(kf[1], qr[0], negm, 0, 0, 0);
;               else if (g & 1) c1 = __builtin_amdgcn_mfma_f32_32x32x16_bf16(kf[g], qr[g >> 1], c1, 0, 0, 0); else c0 = __builtin_amdgcn_mfma_f32_32x32x16_bf16(kf[g], qr[g >> 1], c0, 0, 0, 0);
;               if (g < 8) { const int i = (g >> 1) + 4 * (g & 1); vlo[i] = vtr(vp + (i >> 2) * 4096 + (i & 3) * 1024); vhi[i] = vtr(vp + (i >> 2) * 4096 + (i & 3) * 1024 + 512);
;                   if (g < 4) { sa += pp0[4 * g]; sb += pp0[4 * g + 1]; sa += pp0[4 * g + 2]; sb += pp0[4 * g + 3]; } else { sa += pp1[4 * g - 16]; sb += pp1[4 * g - 15]; sa += pp1[4 * g - 14]; sb += pp1[4 * g - 13]; }
;                   asm volatile("" : "+v"(sa), "+v"(sb)); }
;               { constexpr int G0 = FOX ? 0 : 4; if (g >= G0) { const int q = 2 * (g - G0);
; #pragma unroll
;                   for (int k = 0; k < 2; ++k) { const int w = q + k; const unsigned pkd = w < 8 ? cvt_pk_bf16(pp0[2 * w], pp0[2 * w + 1]) : cvt_pk_bf16(pp1[2 * w - 16], pp1[2 * w - 15]); pw[w >> 2][w & 3] = pkd; } } }
;               SFENCE();
;           }
;           lrun += sa + sb; }
;         MASKONLY(t);
;         float rm; ROWMAX(rm);
;         bool resc = false;
;         if (__any(rm > THR)) { const float dl = fmaxf(rm, 0.f); mhat += dl;
; #pragma unroll
;             for (int r = 0; r < 16; ++r) { c0[r] -= dl; c1[r] -= dl; }
;             if constexpr (!FOX) {
; #pragma unroll
;                 for (int r = 0; r < 16; ++r) negm[r] = -mhat;
.Lmla_ss1_v:
	s_add_i32 s27, s42, 0x6000
	s_and_b32 s27, s27, 0x6000
	s_add_i32 m0, s27, s93
	v_lshl_add_u64 v[4:5], v[232:233], 0, s[42:43]
	global_load_lds_dwordx4 v[4:5], off
	s_add_i32 s27, s42, 0x8000
	v_mfma_f32_32x32x16_bf16 v[114:129], v[206:209], v[138:141], v[82:97]
	s_and_b32 s27, s27, 0x6000
	v_add_u32_e32 v3, s27, v247
	ds_read_b64_tr_b16 v[206:207], v3 offset:49152
	ds_read_b64_tr_b16 v[208:209], v3 offset:49664
	v_add_f32_e32 v4, 0, v67
	v_add_f32_e32 v5, 0, v66
	v_add_f32_e32 v4, v69, v4
	v_add_f32_e32 v5, v68, v5
	v_mfma_f32_32x32x16_bf16 v[98:113], v[194:197], v[138:141], v[82:97]
	ds_read_b64_tr_b16 v[194:195], v3 offset:53248
	ds_read_b64_tr_b16 v[196:197], v3 offset:53760
	v_add_f32_e32 v4, v71, v4
	v_add_f32_e32 v5, v70, v5
	v_add_f32_e32 v4, v73, v4
	v_add_f32_e32 v5, v72, v5
	v_mfma_f32_32x32x16_bf16 v[114:129], v[202:205], v[142:145], v[114:129]
	ds_read_b64_tr_b16 v[202:203], v3 offset:50176
	ds_read_b64_tr_b16 v[204:205], v3 offset:50688
	v_add_f32_e32 v4, v75, v4
	v_add_f32_e32 v5, v74, v5
	v_add_f32_e32 v4, v77, v4
	v_add_f32_e32 v5, v76, v5
	v_mfma_f32_32x32x16_bf16 v[98:113], v[186:189], v[142:145], v[98:113]
	ds_read_b64_tr_b16 v[214:215], v3 offset:54272
	ds_read_b64_tr_b16 v[216:217], v3 offset:54784
	v_add_f32_e32 v4, v79, v4
	v_add_f32_e32 v5, v78, v5
	v_add_f32_e32 v4, v81, v4
	v_add_f32_e32 v5, v80, v5
	v_mfma_f32_32x32x16_bf16 v[114:129], v[198:201], v[146:149], v[114:129]
	ds_read_b64_tr_b16 v[210:211], v3 offset:51200
	ds_read_b64_tr_b16 v[212:213], v3 offset:51712
	v_add_f32_e32 v4, v51, v4
	v_add_f32_e32 v5, v50, v5
	v_add_f32_e32 v4, v53, v4
	v_add_f32_e32 v5, v52, v5
	v_mfma_f32_32x32x16_bf16 v[98:113], v[182:185], v[146:149], v[98:113]
	ds_read_b64_tr_b16 v[12:13], v3 offset:55296
	ds_read_b64_tr_b16 v[14:15], v3 offset:55808
	v_add_f32_e32 v4, v55, v4
	v_add_f32_e32 v5, v54, v5
	v_add_f32_e32 v4, v57, v4
	v_add_f32_e32 v5, v56, v5
	v_mfma_f32_32x32x16_bf16 v[114:129], v[190:193], v[150:153], v[114:129]
	ds_read_b64_tr_b16 v[8:9], v3 offset:52224
	ds_read_b64_tr_b16 v[10:11], v3 offset:52736
	v_add_f32_e32 v4, v59, v4
	v_add_f32_e32 v16, v61, v4
	v_add_f32_e32 v4, v58, v5
	v_add_f32_e32 v17, v60, v4
	v_mfma_f32_32x32x16_bf16 v[98:113], v[170:173], v[150:153], v[98:113]
	ds_read_b64_tr_b16 v[4:5], v3 offset:56320
	ds_read_b64_tr_b16 v[6:7], v3 offset:56832
	v_add_f32_e32 v3, v63, v16
	v_add_f32_e32 v16, v62, v17
	v_add_f32_e32 v3, v65, v3
	v_add_f32_e32 v16, v64, v16
	v_mfma_f32_32x32x16_bf16 v[114:129], v[178:181], v[154:157], v[114:129]
	v_cvt_pk_bf16_f32 v178, v50, v51
	v_cvt_pk_bf16_f32 v179, v52, v53
	v_cvt_pk_bf16_f32 v186, v66, v67
	v_cvt_pk_bf16_f32 v187, v68, v69
	v_mfma_f32_32x32x16_bf16 v[98:113], v[166:169], v[154:157], v[98:113]
	v_cvt_pk_bf16_f32 v180, v54, v55
	v_cvt_pk_bf16_f32 v181, v56, v57
	v_cvt_pk_bf16_f32 v188, v70, v71
	v_cvt_pk_bf16_f32 v189, v72, v73
	v_mfma_f32_32x32x16_bf16 v[114:129], v[174:177], v[158:161], v[114:129]
	v_cvt_pk_bf16_f32 v218, v58, v59
	v_cvt_pk_bf16_f32 v219, v60, v61
	v_cvt_pk_bf16_f32 v182, v74, v75
	v_cvt_pk_bf16_f32 v183, v76, v77
	v_mfma_f32_32x32x16_bf16 v[98:113], v[162:165], v[158:161], v[98:113]
	v_cvt_pk_bf16_f32 v220, v62, v63
	v_cvt_pk_bf16_f32 v221, v64, v65
	v_cvt_pk_bf16_f32 v184, v78, v79
	v_cvt_pk_bf16_f32 v185, v80, v81
	v_add_f32_e32 v3, v3, v16
	v_add_f32_e32 v246, v246, v3
	s_waitcnt lgkmcnt(0)
	v_mfma_f32_32x32x16_bf16 v[18:33], v[186:189], v[206:209], v[18:33]
	s_add_i32 s27, s26, 1
	s_and_b32 s64, s27, 3
	s_mulk_i32 s64, 0x3000
	v_exp_f32_e32 v66, v114
	v_exp_f32_e32 v67, v115
	v_exp_f32_e32 v68, v116
	v_exp_f32_e32 v69, v117
	v_add_u32_e32 v3, s64, v248
	v_mfma_f32_32x32x16_bf16 v[34:49], v[186:189], v[194:197], v[34:49]
	v_exp_f32_e32 v70, v118
	v_exp_f32_e32 v71, v119
	v_exp_f32_e32 v72, v120
	v_exp_f32_e32 v73, v121
	ds_read_b128 v[206:209], v3
	ds_read_b128 v[194:197], v3 offset:512
	v_mfma_f32_32x32x16_bf16 v[18:33], v[182:185], v[202:205], v[18:33]
	v_exp_f32_e32 v74, v122
	v_exp_f32_e32 v75, v123
	v_exp_f32_e32 v76, v124
	v_exp_f32_e32 v77, v125
	ds_read_b128 v[202:205], v3 offset:2048
	ds_read_b128 v[186:189], v3 offset:2560
	v_mfma_f32_32x32x16_bf16 v[34:49], v[182:185], v[214:217], v[34:49]
	v_exp_f32_e32 v78, v126
	v_exp_f32_e32 v79, v127
	v_exp_f32_e32 v80, v128
	v_exp_f32_e32 v81, v129
	ds_read_b128 v[198:201], v3 offset:4096
	ds_read_b128 v[182:185], v3 offset:4608
	v_mfma_f32_32x32x16_bf16 v[18:33], v[178:181], v[210:213], v[18:33]
	v_exp_f32_e32 v50, v98
	v_exp_f32_e32 v51, v99
	v_exp_f32_e32 v52, v100
	v_exp_f32_e32 v53, v101
	ds_read_b128 v[190:193], v3 offset:6144
	ds_read_b128 v[170:173], v3 offset:6656
	v_mfma_f32_32x32x16_bf16 v[34:49], v[178:181], v[12:15], v[34:49]
	v_exp_f32_e32 v54, v102
	v_exp_f32_e32 v55, v103
	v_exp_f32_e32 v56, v104
	v_exp_f32_e32 v57, v105
	ds_read_b128 v[178:181], v3 offset:8192
	ds_read_b128 v[166:169], v3 offset:8704
	v_mfma_f32_32x32x16_bf16 v[18:33], v[218:221], v[8:11], v[18:33]
	v_exp_f32_e32 v58, v106
	v_exp_f32_e32 v59, v107
	v_exp_f32_e32 v60, v108
	v_exp_f32_e32 v61, v109
	ds_read_b128 v[174:177], v3 offset:10240
	ds_read_b128 v[162:165], v3 offset:10752
	v_mfma_f32_32x32x16_bf16 v[34:49], v[218:221], v[4:7], v[34:49]
	v_exp_f32_e32 v62, v110
	v_exp_f32_e32 v63, v111
	v_exp_f32_e32 v64, v112
	v_exp_f32_e32 v65, v113
	s_waitcnt vmcnt(4)
	s_waitcnt lgkmcnt(0)
	s_barrier
	s_add_u32 s42, s42, 0x2000
	s_addc_u32 s43, s43, 0
	v_lshl_add_u64 v[234:235], v[234:235], 0, s[62:63]
	s_mov_b32 s26, s27
	s_cmp_lt_u32 s27, s47
	s_cbranch_scc1 .Lmla_ss1_top
	s_cmp_eq_u32 s27, s96
	s_cbranch_scc1 .Lmla_ss_done
	s_branch .Lmla_ss_back

; template <bool FOX>
; __device__ __forceinline__ void attn_unit(const Args& A, int b, int h, int qb, LAS char* shm, LAS float* dg) {
;     ...
;     for (int t = 1; t < t_end; ++t) {
;         if (t == 1 && 4 < nti) ISSUE_K(t0 + 4, 0);
;         if (t + 4 < nti) ISSUE_K(t0 + t + 4, t % NS);
;         if (t + 2 < nti) ISSUE_V(t0 + t + 2, (t + 2) % NS);
;         SFENCE();
;         { if constexpr (!FOX) { if (t0 + t == tw_last + 1) {
; #pragma unroll
;                   for (int r = 0; r < 16; ++r) negm[r] = -INFINITY;
;                   asm volatile("" : "+v"(negm)); } }
;           const lds_cptr vp = vp0 + ((t - 1) % NS) * VSLOT; float sa = 0.f, sb = 0.f;
; #pragma unroll
;           for (int g = 0; g < 2 * NQ; ++g) {
;               if (!FOX && g == 0) c0 = __builtin_amdgcn_mfma_f32_32x32x16_bf16(kf[0], qr[0], negm, 0, 0, 0);
;               else if (!FOX && g == 1) c1 = __builtin_amdgcn_mfma_f32_32x32x16_bf16(kf[1], qr[0], negm, 0, 0, 0);
;               else if (g & 1) c1 = __builtin_amdgcn_mfma_f32_32x32x16_bf16(kf[g], qr[g >> 1], c1, 0, 0, 0); else c0 = __builtin_amdgcn_mfma_f32_32x32x16_bf16(kf[g], qr[g >> 1], c0, 0, 0, 0);
;               if (g < 8) { const int i = (g >> 1) + 4 * (g & 1); vlo[i] = vtr(vp + (i >> 2) * 4096 + (i & 3) * 1024); vhi[i] = vtr(vp + (i >> 2) * 4096 + (i & 3) * 1024 + 512);
;                   if (g < 4) { sa += pp0[4 * g]; sb += pp0[4 * g + 1]; sa += pp0[4 * g + 2]; sb += pp0[4 * g + 3]; } else { sa += pp1[4 * g - 16]; sb += pp1[4 * g - 15]; sa += pp1[4 * g - 14]; sb += pp1[4 * g - 13]; }
;                   asm volatile("" : "+v"(sa), "+v"(sb)); }
;               { constexpr int G0 = FOX ? 0 : 4; if (g >= G0) { const int q = 2 * (g - G0);
; #pragma unroll
;                   for (int k = 0; k < 2; ++k) { const int w = q + k; const unsigned pkd = w < 8 ? cvt_pk_bf16(pp0[2 * w], pp0[2 * w + 1]) : cvt_pk_bf16(pp1[2 * w - 16], pp1[2 * w - 15]); pw[w >> 2][w & 3] = pkd; } } }
;               SFENCE();
;           }
;           lrun += sa + sb; }
;         MASKONLY(t);
;         float rm; ROWMAX(rm);
;         bool resc = false;
;         if (__any(rm > THR)) { const float dl = fmaxf(rm, 0.f); mhat += dl;
; #pragma unroll
;             for (int r = 0; r < 16; ++r) { c0[r] -= dl; c1[r] -= dl; }
;             if constexpr (!FOX) {
; #pragma unroll
;                 for (int r = 0; r < 16; ++r) negm[r] = -mhat;
.Lmla_ss2_v:
	s_add_i32 s27, s42, 0x6000
	s_and_b32 s27, s27, 0x6000
	s_add_i32 m0, s27, s93
	v_lshl_add_u64 v[4:5], v[232:233], 0, s[42:43]
	global_load_lds_dwordx4 v[4:5], off
	s_add_i32 s27, s42, 0x8000
	v_mfma_f32_32x32x16_bf16 v[114:129], v[206:209], v[138:141], v[82:97]
	s_and_b32 s27, s27, 0x6000
	v_add_u32_e32 v3, s27, v247
	ds_read_b64_tr_b16 v[206:207], v3 offset:49152
	ds_read_b64_tr_b16 v[208:209], v3 offset:49664
	v_add_f32_e32 v4, 0, v67
	v_add_f32_e32 v5, 0, v66
	v_add_f32_e32 v4, v69, v4
	v_add_f32_e32 v5, v68, v5
	v_mfma_f32_32x32x16_bf16 v[98:113], v[194:197], v[138:141], v[82:97]
	ds_read_b64_tr_b16 v[194:195], v3 offset:53248
	ds_read_b64_tr_b16 v[196:197], v3 offset:53760
	v_add_f32_e32 v4, v71, v4
	v_add_f32_e32 v5, v70, v5
	v_add_f32_e32 v4, v73, v4
	v_add_f32_e32 v5, v72, v5
	v_mfma_f32_32x32x16_bf16 v[114:129], v[202:205], v[142:145], v[114:129]
	ds_read_b64_tr_b16 v[202:203], v3 offset:50176
	ds_read_b64_tr_b16 v[204:205], v3 offset:50688
	v_add_f32_e32 v4, v75, v4
	v_add_f32_e32 v5, v74, v5
	v_add_f32_e32 v4, v77, v4
	v_add_f32_e32 v5, v76, v5
	v_mfma_f32_32x32x16_bf16 v[98:113], v[186:189], v[142:145], v[98:113]
	ds_read_b64_tr_b16 v[214:215], v3 offset:54272
	ds_read_b64_tr_b16 v[216:217], v3 offset:54784
	v_add_f32_e32 v4, v79, v4
	v_add_f32_e32 v5, v78, v5
	v_add_f32_e32 v4, v81, v4
	v_add_f32_e32 v5, v80, v5
	v_mfma_f32_32x32x16_bf16 v[114:129], v[198:201], v[146:149], v[114:129]
	ds_read_b64_tr_b16 v[210:211], v3 offset:51200
	ds_read_b64_tr_b16 v[212:213], v3 offset:51712
	v_add_f32_e32 v4, v51, v4
	v_add_f32_e32 v5, v50, v5
	v_add_f32_e32 v4, v53, v4
	v_add_f32_e32 v5, v52, v5
	v_mfma_f32_32x32x16_bf16 v[98:113], v[182:185], v[146:149], v[98:113]
	ds_read_b64_tr_b16 v[12:13], v3 offset:55296
	ds_read_b64_tr_b16 v[14:15], v3 offset:55808
	v_add_f32_e32 v4, v55, v4
	v_add_f32_e32 v5, v54, v5
	v_add_f32_e32 v4, v57, v4
	v_add_f32_e32 v5, v56, v5
	v_mfma_f32_32x32x16_bf16 v[114:129], v[190:193], v[150:153], v[114:129]
	ds_read_b64_tr_b16 v[8:9], v3 offset:52224
	ds_read_b64_tr_b16 v[10:11], v3 offset:52736
	v_add_f32_e32 v4, v59, v4
	v_add_f32_e32 v16, v61, v4
	v_add_f32_e32 v4, v58, v5
	v_add_f32_e32 v17, v60, v4
	v_mfma_f32_32x32x16_bf16 v[98:113], v[170:173], v[150:153], v[98:113]
	ds_read_b64_tr_b16 v[4:5], v3 offset:56320
	ds_read_b64_tr_b16 v[6:7], v3 offset:56832
	v_add_f32_e32 v3, v63, v16
	v_add_f32_e32 v16, v62, v17
	v_add_f32_e32 v3, v65, v3
	v_add_f32_e32 v16, v64, v16
	v_mfma_f32_32x32x16_bf16 v[114:129], v[178:181], v[154:157], v[114:129]
	v_cvt_pk_bf16_f32 v178, v50, v51
	v_cvt_pk_bf16_f32 v179, v52, v53
	v_cvt_pk_bf16_f32 v186, v66, v67
	v_cvt_pk_bf16_f32 v187, v68, v69
	v_mfma_f32_32x32x16_bf16 v[98:113], v[166:169], v[154:157], v[98:113]
	v_cvt_pk_bf16_f32 v180, v54, v55
	v_cvt_pk_bf16_f32 v181, v56, v57
	v_cvt_pk_bf16_f32 v188, v70, v71
	v_cvt_pk_bf16_f32 v189, v72, v73
	v_mfma_f32_32x32x16_bf16 v[114:129], v[174:177], v[158:161], v[114:129]
	v_cvt_pk_bf16_f32 v218, v58, v59
	v_cvt_pk_bf16_f32 v219, v60, v61
	v_cvt_pk_bf16_f32 v182, v74, v75
	v_cvt_pk_bf16_f32 v183, v76, v77
	v_mfma_f32_32x32x16_bf16 v[98:113], v[162:165], v[158:161], v[98:113]
	v_cvt_pk_bf16_f32 v220, v62, v63
	v_cvt_pk_bf16_f32 v221, v64, v65
	v_cvt_pk_bf16_f32 v184, v78, v79
	v_cvt_pk_bf16_f32 v185, v80, v81
	v_add_f32_e32 v3, v3, v16
	v_add_f32_e32 v246, v246, v3
	s_waitcnt vmcnt(3)
	s_waitcnt lgkmcnt(0)
	s_barrier
	v_mfma_f32_32x32x16_bf16 v[18:33], v[186:189], v[206:209], v[18:33]
	s_add_i32 s27, s26, 1
	s_and_b32 s64, s27, 3
	s_mulk_i32 s64, 0x3000
	v_exp_f32_e32 v66, v114
	v_exp_f32_e32 v67, v115
	v_exp_f32_e32 v68, v116
	v_exp_f32_e32 v69, v117
	v_add_u32_e32 v3, s64, v248
	v_mfma_f32_32x32x16_bf16 v[34:49], v[186:189], v[194:197], v[34:49]
	v_exp_f32_e32 v70, v118
	v_exp_f32_e32 v71, v119
	v_exp_f32_e32 v72, v120
	v_exp_f32_e32 v73, v121
	ds_read_b128 v[206:209], v3
	ds_read_b128 v[194:197], v3 offset:512
	v_mfma_f32_32x32x16_bf16 v[18:33], v[182:185], v[202:205], v[18:33]
	v_exp_f32_e32 v74, v122
	v_exp_f32_e32 v75, v123
	v_exp_f32_e32 v76, v124
	v_exp_f32_e32 v77, v125
	ds_read_b128 v[202:205], v3 offset:2048
	ds_read_b128 v[186:189], v3 offset:2560
	v_mfma_f32_32x32x16_bf16 v[34:49], v[182:185], v[214:217], v[34:49]
	v_exp_f32_e32 v78, v126
	v_exp_f32_e32 v79, v127
	v_exp_f32_e32 v80, v128
	v_exp_f32_e32 v81, v129
	ds_read_b128 v[198:201], v3 offset:4096
	ds_read_b128 v[182:185], v3 offset:4608
	v_mfma_f32_32x32x16_bf16 v[18:33], v[178:181], v[210:213], v[18:33]
	v_exp_f32_e32 v50, v98
	v_exp_f32_e32 v51, v99
	v_exp_f32_e32 v52, v100
	v_exp_f32_e32 v53, v101
	ds_read_b128 v[190:193], v3 offset:6144
	ds_read_b128 v[170:173], v3 offset:6656
	v_mfma_f32_32x32x16_bf16 v[34:49], v[178:181], v[12:15], v[34:49]
	v_exp_f32_e32 v54, v102
	v_exp_f32_e32 v55, v103
	v_exp_f32_e32 v56, v104
	v_exp_f32_e32 v57, v105
	ds_read_b128 v[178:181], v3 offset:8192
	ds_read_b128 v[166:169], v3 offset:8704
	v_mfma_f32_32x32x16_bf16 v[18:33], v[218:221], v[8:11], v[18:33]
	v_exp_f32_e32 v58, v106
	v_exp_f32_e32 v59, v107
	v_exp_f32_e32 v60, v108
	v_exp_f32_e32 v61, v109
	ds_read_b128 v[174:177], v3 offset:10240
	ds_read_b128 v[162:165], v3 offset:10752
	v_mfma_f32_32x32x16_bf16 v[34:49], v[218:221], v[4:7], v[34:49]
	v_exp_f32_e32 v62, v110
	v_exp_f32_e32 v63, v111
	v_exp_f32_e32 v64, v112
	v_exp_f32_e32 v65, v113
	s_waitcnt lgkmcnt(0)
	s_add_u32 s42, s42, 0x2000
	s_addc_u32 s43, s43, 0
	v_lshl_add_u64 v[234:235], v[234:235], 0, s[62:63]
	s_mov_b32 s26, s27
	s_cmp_lt_u32 s27, s47
	s_cbranch_scc1 .Lmla_ss2_top
	s_cmp_eq_u32 s27, s96
	s_cbranch_scc1 .Lmla_ss_done
	s_branch .Lmla_ss_back
